# baseline (speedup 1.0000x reference)
_Z10giou_finalPK15HIP_vector_typeIfLj2EEPf:
	s_load_dwordx4 s[12:15], s[0:1], 0x0
	v_lshlrev_b32_e32 v1, 4, v0
	v_cmp_eq_u32_e32 vcc, 0, v0
	v_mov_b32_e32 v18, 0
	s_waitcnt lgkmcnt(0)
	global_load_dwordx4 v[2:5], v1, s[12:13]
	global_load_dwordx4 v[6:9], v1, s[12:13] offset:1024
	global_load_dwordx4 v[10:13], v1, s[12:13] offset:2048
	global_load_dwordx4 v[14:17], v1, s[12:13] offset:3072
	s_mov_b64 exec, 1
	global_load_dword v19, v18, s[14:15]
	s_mov_b64 exec, -1
	s_waitcnt vmcnt(4)
	v_add_f32_e32 v1, v2, v4
	v_add_f32_e32 v2, v3, v5
	s_waitcnt vmcnt(3)
	v_add_f32_e32 v3, v6, v8
	v_add_f32_e32 v4, v7, v9
	v_add_f32_e32 v1, 0, v1
	v_add_f32_e32 v2, 0, v2
	s_waitcnt vmcnt(2)
	v_add_f32_e32 v5, v10, v12
	v_add_f32_e32 v6, v11, v13
	v_add_f32_e32 v1, v1, v3
	v_add_f32_e32 v2, v2, v4
	s_waitcnt vmcnt(1)
	v_add_f32_e32 v7, v14, v16
	v_add_f32_e32 v8, v15, v17
	v_add_f32_e32 v1, v1, v5
	v_add_f32_e32 v2, v2, v6
	v_add_f32_e32 v1, v1, v7
	v_add_f32_e32 v2, v2, v8
	s_nop 0
	v_add_f32_dpp v1, v1, v1 quad_perm:[1,0,3,2] row_mask:0xf bank_mask:0xf bound_ctrl:1
	v_add_f32_dpp v2, v2, v2 quad_perm:[1,0,3,2] row_mask:0xf bank_mask:0xf bound_ctrl:1
	s_nop 0
	v_add_f32_dpp v1, v1, v1 quad_perm:[2,3,0,1] row_mask:0xf bank_mask:0xf bound_ctrl:1
	v_add_f32_dpp v2, v2, v2 quad_perm:[2,3,0,1] row_mask:0xf bank_mask:0xf bound_ctrl:1
	s_nop 0
	v_add_f32_dpp v1, v1, v1 row_half_mirror row_mask:0xf bank_mask:0xf bound_ctrl:1
	v_add_f32_dpp v2, v2, v2 row_half_mirror row_mask:0xf bank_mask:0xf bound_ctrl:1
	s_nop 0
	v_add_f32_dpp v1, v1, v1 row_mirror row_mask:0xf bank_mask:0xf bound_ctrl:1
	v_add_f32_dpp v2, v2, v2 row_mirror row_mask:0xf bank_mask:0xf bound_ctrl:1
	v_readlane_b32 s2, v1, 0
	v_readlane_b32 s5, v1, 16
	v_readlane_b32 s3, v1, 32
	v_readlane_b32 s4, v1, 48
	v_readlane_b32 s6, v2, 0
	v_readlane_b32 s9, v2, 16
	v_readlane_b32 s7, v2, 32
	v_readlane_b32 s8, v2, 48
	s_and_saveexec_b64 s[10:11], vcc
	s_cbranch_execz .LBB1_2
	v_mov_b32_e32 v0, s9
	v_add_f32_e32 v0, s6, v0
	v_mov_b32_e32 v1, s5
	v_add_f32_e32 v0, s7, v0
	v_add_f32_e32 v1, s2, v1
	v_add_f32_e32 v0, s8, v0
	v_add_f32_e32 v1, s3, v1
	v_add_f32_e32 v1, s4, v1
	v_max_f32_e32 v0, 1.0, v0
	v_div_scale_f32 v2, s[2:3], v0, v0, v1
	v_rcp_f32_e32 v3, v2
	s_nop 0
	v_fma_f32 v4, -v2, v3, 1.0
	v_fmac_f32_e32 v3, v4, v3
	v_div_scale_f32 v4, vcc, v1, v0, v1
	v_mul_f32_e32 v5, v4, v3
	v_fma_f32 v6, -v2, v5, v4
	v_fmac_f32_e32 v5, v6, v3
	v_fma_f32 v2, -v2, v5, v4
	v_div_fmas_f32 v2, v2, v3, v5
	v_div_fixup_f32 v0, v2, v0, v1
	v_mov_b32_e32 v1, 0
	global_store_dword v1, v0, s[14:15]

	.amdhsa_kernel _Z10giou_finalPK15HIP_vector_typeIfLj2EEPf
		.amdhsa_group_segment_fixed_size 0
		.amdhsa_private_segment_fixed_size 0
		.amdhsa_kernarg_size 16
		.amdhsa_user_sgpr_count 2
		.amdhsa_user_sgpr_dispatch_ptr 0
		.amdhsa_user_sgpr_queue_ptr 0
		.amdhsa_user_sgpr_kernarg_segment_ptr 1
		.amdhsa_user_sgpr_dispatch_id 0
		.amdhsa_user_sgpr_kernarg_preload_length 0
		.amdhsa_user_sgpr_kernarg_preload_offset 0
		.amdhsa_user_sgpr_private_segment_size 0
		.amdhsa_uses_dynamic_stack 0
		.amdhsa_enable_private_segment 0
		.amdhsa_system_sgpr_workgroup_id_x 1
		.amdhsa_system_sgpr_workgroup_id_y 0
		.amdhsa_system_sgpr_workgroup_id_z 0
		.amdhsa_system_sgpr_workgroup_info 0
		.amdhsa_system_vgpr_workitem_id 0
		.amdhsa_next_free_vgpr 20
		.amdhsa_next_free_sgpr 16
		.amdhsa_accum_offset 20
		.amdhsa_reserve_vcc 1
		.amdhsa_float_round_mode_32 0
		.amdhsa_float_round_mode_16_64 0
		.amdhsa_float_denorm_mode_32 3
		.amdhsa_float_denorm_mode_16_64 3
		.amdhsa_dx10_clamp 1
		.amdhsa_ieee_mode 1
		.amdhsa_fp16_overflow 0
		.amdhsa_tg_split 0
		.amdhsa_exception_fp_ieee_invalid_op 0
		.amdhsa_exception_fp_denorm_src 0
		.amdhsa_exception_fp_ieee_div_zero 0
		.amdhsa_exception_fp_ieee_overflow 0
		.amdhsa_exception_fp_ieee_underflow 0
		.amdhsa_exception_fp_ieee_inexact 0
		.amdhsa_exception_int_div_zero 0
	.end_amdhsa_kernel

.Lfunc_end1:
	.size	_Z10giou_finalPK15HIP_vector_typeIfLj2EEPf, .Lfunc_end1-_Z10giou_finalPK15HIP_vector_typeIfLj2EEPf
	.set _Z10giou_finalPK15HIP_vector_typeIfLj2EEPf.num_vgpr, 20
	.set _Z10giou_finalPK15HIP_vector_typeIfLj2EEPf.num_agpr, 0
	.set _Z10giou_finalPK15HIP_vector_typeIfLj2EEPf.numbered_sgpr, 16
	.set _Z10giou_finalPK15HIP_vector_typeIfLj2EEPf.num_named_barrier, 0
	.set _Z10giou_finalPK15HIP_vector_typeIfLj2EEPf.private_seg_size, 0
	.set _Z10giou_finalPK15HIP_vector_typeIfLj2EEPf.uses_vcc, 1
	.set _Z10giou_finalPK15HIP_vector_typeIfLj2EEPf.uses_flat_scratch, 0
	.set _Z10giou_finalPK15HIP_vector_typeIfLj2EEPf.has_dyn_sized_stack, 0
	.set _Z10giou_finalPK15HIP_vector_typeIfLj2EEPf.has_recursion, 0
	.set _Z10giou_finalPK15HIP_vector_typeIfLj2EEPf.has_indirect_call, 0

amdhsa.kernels:
  - .agpr_count:     0
    .args:
      - .actual_access:  read_only
        .address_space:  global
        .offset:         0
        .size:           8
        .value_kind:     global_buffer
      - .actual_access:  read_only
        .address_space:  global
        .offset:         8
        .size:           8
        .value_kind:     global_buffer
      - .actual_access:  read_only
        .address_space:  global
        .offset:         16
        .size:           8
        .value_kind:     global_buffer
      - .actual_access:  read_only
        .address_space:  global
        .offset:         24
        .size:           8
        .value_kind:     global_buffer
      - .actual_access:  write_only
        .address_space:  global
        .offset:         32
        .size:           8
        .value_kind:     global_buffer
    .group_segment_fixed_size: 24704
    .kernarg_segment_align: 8
    .kernarg_segment_size: 40
    .language:       OpenCL C
    .language_version:
      - 2
      - 0
    .max_flat_workgroup_size: 1024
    .name:           _Z12giou_partialPK15HIP_vector_typeIfLj4EES2_S2_PKiPS_IfLj2EE
    .private_segment_fixed_size: 0
    .sgpr_count:     32
    .sgpr_spill_count: 0
    .symbol:         _Z12giou_partialPK15HIP_vector_typeIfLj4EES2_S2_PKiPS_IfLj2EE.kd
    .uniform_work_group_size: 1
    .uses_dynamic_stack: false
    .vgpr_count:     24
    .vgpr_spill_count: 0
    .wavefront_size: 64
  - .agpr_count:     0
    .args:
      - .actual_access:  read_only
        .address_space:  global
        .offset:         0
        .size:           8
        .value_kind:     global_buffer
      - .actual_access:  write_only
        .address_space:  global
        .offset:         8
        .size:           8
        .value_kind:     global_buffer
    .group_segment_fixed_size: 0
    .kernarg_segment_align: 8
    .kernarg_segment_size: 16
    .language:       OpenCL C
    .language_version:
      - 2
      - 0
    .max_flat_workgroup_size: 64
    .name:           _Z10giou_finalPK15HIP_vector_typeIfLj2EEPf
    .private_segment_fixed_size: 0
    .sgpr_count:     22
    .sgpr_spill_count: 0
    .symbol:         _Z10giou_finalPK15HIP_vector_typeIfLj2EEPf.kd
    .uniform_work_group_size: 1
    .uses_dynamic_stack: false
    .vgpr_count:     20
    .vgpr_spill_count: 0
    .wavefront_size: 64
